# P9 K-loop: leading wave group takes its two 6-count waits one interval later (end of its own following MFMA interval): one more interval of latency tolerance for the pieces it stages
# speedup vs baseline: 1.0047x; 1.0047x over previous
; #define PG8_STAGE(bufoff, gbase, voff) do { PG8_GLDS((const char*)(gbase), (voff)[0], ldsb + (bufoff)); PG8_GLDS((const char*)(gbase), (voff)[1], ldsb + (bufoff) + 8192u); } while (0)
; #define PG8_STAGEA(bufoff, gbase, o0, o1) do { PG8_GLDS((const char*)(gbase), (o0), ldsb + (bufoff)); PG8_GLDS((const char*)(gbase), (o1), ldsb + (bufoff) + 8192u); } while (0)
; #define PG8_LDA(dst, b, h) do { if constexpr (F8) { _Pragma("unroll") for (int m = 0; m < 4; ++m) dst##8[m] = PG8_LD32(lds + PG8_SA(b, h) + aoff + m * 2048); } else { \
;         _Pragma("unroll") for (int m = 0; m < 4; ++m) _Pragma("unroll") for (int k = 0; k < 2; ++k) dst[m][k] = *(const LAS bf16x8*)(lds + PG8_SA(b, h) + aoff + m * 2048 + k * 1024); } } while (0)
; #define PG8_WAIT_VX() do { if (relax) asm volatile("s_waitcnt vmcnt(%0)" :: "n"(8 + Epi::RELAX) : "memory"); else PG8_WAIT_V(8); } while (0)
; #define PG8_WAIT_L(n) asm volatile("s_waitcnt lgkmcnt(" #n ")" ::: "memory")
; #define PG8_BAR __builtin_amdgcn_s_barrier()
; #define PG8_SCHED __builtin_amdgcn_sched_barrier(0)
; template <class Epi, class Sched, bool F8 = false, bool PF = false, bool I8 = false, int PID = -1>
; __device__ __forceinline__ void gemm_phase(LAS unsigned char* lds, LAS unsigned char* xlds, const int RP, const int RPB, const int nt, const Sched& S, const Epi& E, const int stagger_ticks) {
;     ...
;             PG8_LDA(At, 0, 1); PG8_STAGE(PG8_SB(0, 0), b2, voffB); PG8_STAGE(PG8_SB(0, 1), b2 + hstepB, voffB); PG8_STAGEA(PG8_SA(0, 0), a2, vA0, vA1);
;             PG8_WAIT_VX(); PG8_WAIT_L(0); PG8_BAR; PG8_MMA(1, 0, At, B0); PG8_MMA(1, 1, At, B1); PG8_BAR; PG8_SCHED;
.LBB0_1062:
	s_add_u32 s30, s26, 0xfffe0080
	s_addc_u32 s31, s27, -1
	s_cmp_eq_u32 s73, 4
	s_cselect_b32 s38, s6, s30
	s_cselect_b32 s39, s7, s31
	s_cselect_b32 s34, s8, s25
	s_cselect_b32 s35, s9, s71
	s_add_u32 s30, s38, 0x80
	s_addc_u32 s31, s39, 0
	s_add_u32 s36, s34, 0x80
	s_addc_u32 s37, s35, 0
	ds_read_b128 v[170:173], v169 offset:16384
	ds_read_b128 v[174:177], v169 offset:17408
	ds_read_b128 v[178:181], v169 offset:18432
	ds_read_b128 v[182:185], v169 offset:19456
	ds_read_b128 v[186:189], v169 offset:20480
	ds_read_b128 v[190:193], v169 offset:21504
	ds_read_b128 v[194:197], v169 offset:22528
	ds_read_b128 v[198:201], v169 offset:23552
	s_add_i32 s75, s74, 0x10000
	s_mov_b32 m0, s75
	s_nop 0
	global_load_lds_dwordx4 v166, s[34:35]
	s_add_i32 s75, s74, 0x12000
	s_mov_b32 m0, s75
	s_nop 0
	global_load_lds_dwordx4 v167, s[34:35]
	s_add_u32 s76, s34, 0x2000
	s_addc_u32 s77, s35, 0
	s_add_i32 s75, s74, 0x14000
	s_mov_b32 m0, s75
	s_nop 0
	global_load_lds_dwordx4 v166, s[76:77]
	s_add_i32 s75, s74, 0x16000
	s_mov_b32 m0, s75
	s_nop 0
	global_load_lds_dwordx4 v167, s[76:77]
	s_and_b64 vcc, exec, s[18:19]
	s_cbranch_vccnz .Lmy_w9a0
	s_waitcnt vmcnt(6)
.Lmy_w9a0:
	s_waitcnt lgkmcnt(0)
	s_barrier
	s_setprio 1
	s_waitcnt lgkmcnt(6)
	v_mfma_f32_16x16x128_f8f6f4 v[86:89], v[2:9], v[170:177], v[86:89]
	v_mfma_f32_16x16x128_f8f6f4 v[82:85], v[10:17], v[170:177], v[82:85]
	s_waitcnt lgkmcnt(4)
	v_mfma_f32_16x16x128_f8f6f4 v[70:73], v[2:9], v[178:185], v[70:73]
	v_mfma_f32_16x16x128_f8f6f4 v[66:69], v[10:17], v[178:185], v[66:69]
	s_waitcnt lgkmcnt(2)
	v_mfma_f32_16x16x128_f8f6f4 v[202:205], v[2:9], v[186:193], v[54:57]
	v_mfma_f32_16x16x128_f8f6f4 v[206:209], v[10:17], v[186:193], v[50:53]
	s_waitcnt lgkmcnt(0)
	v_mfma_f32_16x16x128_f8f6f4 v[210:213], v[2:9], v[194:201], v[38:41]
	v_mfma_f32_16x16x128_f8f6f4 v[214:217], v[10:17], v[194:201], v[34:37]
	v_mfma_f32_16x16x128_f8f6f4 v[94:97], v[18:25], v[170:177], v[94:97]
	v_mfma_f32_16x16x128_f8f6f4 v[90:93], v[26:33], v[170:177], v[90:93]
	v_mfma_f32_16x16x128_f8f6f4 v[78:81], v[18:25], v[178:185], v[78:81]
	v_mfma_f32_16x16x128_f8f6f4 v[74:77], v[26:33], v[178:185], v[74:77]
	v_mfma_f32_16x16x128_f8f6f4 v[218:221], v[18:25], v[186:193], v[62:65]
	v_mfma_f32_16x16x128_f8f6f4 v[186:189], v[26:33], v[186:193], v[58:61]
	v_mfma_f32_16x16x128_f8f6f4 v[190:193], v[18:25], v[194:201], v[46:49]
	v_mfma_f32_16x16x128_f8f6f4 v[194:197], v[26:33], v[194:201], v[42:45]
	s_setprio 0
	s_and_b64 vcc, exec, s[18:19]
	s_cbranch_vccz .Lmy_w9b0
	s_waitcnt vmcnt(6)
; #define PG8_STAGE(bufoff, gbase, voff) do { PG8_GLDS((const char*)(gbase), (voff)[0], ldsb + (bufoff)); PG8_GLDS((const char*)(gbase), (voff)[1], ldsb + (bufoff) + 8192u); } while (0)
; #define PG8_STAGEA(bufoff, gbase, o0, o1) do { PG8_GLDS((const char*)(gbase), (o0), ldsb + (bufoff)); PG8_GLDS((const char*)(gbase), (o1), ldsb + (bufoff) + 8192u); } while (0)
; #define PG8_STAGEA1(bufoff, gbase) do { if constexpr (Sched::GATHER) { PG8_STAGEA(bufoff, gbase, vA2, vA3); } else { PG8_STAGEA(bufoff, (gbase) + hstep, vA0, vA1); } } while (0)
; #define PG8_LDA(dst, b, h) do { if constexpr (F8) { _Pragma("unroll") for (int m = 0; m < 4; ++m) dst##8[m] = PG8_LD32(lds + PG8_SA(b, h) + aoff + m * 2048); } else { \
;         _Pragma("unroll") for (int m = 0; m < 4; ++m) _Pragma("unroll") for (int k = 0; k < 2; ++k) dst[m][k] = *(const LAS bf16x8*)(lds + PG8_SA(b, h) + aoff + m * 2048 + k * 1024); } } while (0)
; #define PG8_LDB(dst, b, h) do { if constexpr (F8) { _Pragma("unroll") for (int n = 0; n < 2; ++n) dst##8[n] = PG8_LD32(lds + PG8_SB(b, h) + boff + n * 2048); } else { \
;         _Pragma("unroll") for (int n = 0; n < 2; ++n) _Pragma("unroll") for (int k = 0; k < 2; ++k) dst[n][k] = *(const LAS bf16x8*)(lds + PG8_SB(b, h) + boff + n * 2048 + k * 1024); } } while (0)
; #define PG8_WAIT_VR() PG8_WAIT_V(8)
; #define PG8_WAIT_VX() do { if (relax) asm volatile("s_waitcnt vmcnt(%0)" :: "n"(8 + Epi::RELAX) : "memory"); else PG8_WAIT_V(8); } while (0)
; template <class Epi, class Sched, bool F8 = false, bool PF = false, bool I8 = false, int PID = -1>
; __device__ __forceinline__ void gemm_phase(LAS unsigned char* lds, LAS unsigned char* xlds, const int RP, const int RPB, const int nt, const Sched& S, const Epi& E, const int stagger_ticks) {
;     ...
;             PG8_WAIT_VX(); PG8_WAIT_L(0); PG8_BAR; PG8_MMA(1, 0, At, B0); PG8_MMA(1, 1, At, B1); PG8_BAR; PG8_SCHED;
;             PG8_LDB(B0, 1, 0); PG8_LDB(B1, 1, 1); PG8_SCHED; PG8_LDA(At, 1, 0); PG8_STAGEA1(PG8_SA(0, 1), a2);
;             PG8_WAIT_VR(); PG8_WAIT_L(0); PG8_BAR; PG8_MMA(0, 0, At, B0); PG8_MMA(0, 1, At, B1); PG8_BAR; PG8_SCHED;
;             PG8_LDA(At, 1, 1); PG8_STAGE(PG8_SB(1, 0), b3, voffB); PG8_STAGE(PG8_SB(1, 1), b3 + hstepB, voffB); PG8_STAGEA(PG8_SA(1, 0), a3, vA0, vA1);
;             PG8_WAIT_VR(); PG8_WAIT_L(0); PG8_BAR; PG8_MMA(1, 0, At, B0); PG8_MMA(1, 1, At, B1); PG8_BAR; PG8_SCHED;
;         }
.Lmy_w9b0:
	s_barrier
	s_add_i32 s75, s74, 0x2000
	s_mov_b32 m0, s74
	s_nop 0
	global_load_lds_dwordx4 v164, s[38:39]
	s_nop 0
	s_mov_b32 m0, s75
	s_nop 0
	global_load_lds_dwordx4 v165, s[38:39]
	v_add_u32_e32 v14, 0x18000, v168
	v_add_u32_e32 v30, 0x1c000, v168
	ds_read_b128 v[2:5], v14
	ds_read_b128 v[6:9], v14 offset:1024
	ds_read_b128 v[10:13], v14 offset:2048
	ds_read_b128 v[14:17], v14 offset:3072
	ds_read_b128 v[18:21], v30
	ds_read_b128 v[22:25], v30 offset:1024
	ds_read_b128 v[26:29], v30 offset:2048
	ds_read_b128 v[30:33], v30 offset:3072
	ds_read_b128 v[34:37], v169 offset:32768
	ds_read_b128 v[38:41], v169 offset:33792
	ds_read_b128 v[42:45], v169 offset:34816
	ds_read_b128 v[46:49], v169 offset:35840
	ds_read_b128 v[50:53], v169 offset:36864
	ds_read_b128 v[54:57], v169 offset:37888
	ds_read_b128 v[58:61], v169 offset:38912
	ds_read_b128 v[62:65], v169 offset:39936
	s_add_u32 s38, s38, 0x20000
	s_addc_u32 s39, s39, 0
	s_add_i32 s75, s74, 0x4000
	s_mov_b32 m0, s75
	s_nop 0
	global_load_lds_dwordx4 v164, s[38:39]
	s_add_i32 s75, s74, 0x6000
	s_mov_b32 m0, s75
	s_nop 0
	global_load_lds_dwordx4 v165, s[38:39]
	s_waitcnt vmcnt(8)
	s_waitcnt lgkmcnt(0)
	s_barrier
	s_setprio 1
	s_waitcnt lgkmcnt(6)
	v_mfma_f32_16x16x128_f8f6f4 v[150:153], v[2:9], v[34:41], v[150:153]
	v_mfma_f32_16x16x128_f8f6f4 v[146:149], v[10:17], v[34:41], v[146:149]
	s_waitcnt lgkmcnt(4)
	v_mfma_f32_16x16x128_f8f6f4 v[134:137], v[2:9], v[42:49], v[134:137]
	v_mfma_f32_16x16x128_f8f6f4 v[130:133], v[10:17], v[42:49], v[130:133]
	s_waitcnt lgkmcnt(2)
	v_mfma_f32_16x16x128_f8f6f4 v[118:121], v[2:9], v[50:57], v[118:121]
	v_mfma_f32_16x16x128_f8f6f4 v[114:117], v[10:17], v[50:57], v[114:117]
	s_waitcnt lgkmcnt(0)
	v_mfma_f32_16x16x128_f8f6f4 v[102:105], v[2:9], v[58:65], v[102:105]
	v_mfma_f32_16x16x128_f8f6f4 v[98:101], v[10:17], v[58:65], v[98:101]
	v_mfma_f32_16x16x128_f8f6f4 v[158:161], v[18:25], v[34:41], v[158:161]
	v_mfma_f32_16x16x128_f8f6f4 v[154:157], v[26:33], v[34:41], v[154:157]
	v_mfma_f32_16x16x128_f8f6f4 v[142:145], v[18:25], v[42:49], v[142:145]
	v_mfma_f32_16x16x128_f8f6f4 v[138:141], v[26:33], v[42:49], v[138:141]
	v_mfma_f32_16x16x128_f8f6f4 v[126:129], v[18:25], v[50:57], v[126:129]
	v_mfma_f32_16x16x128_f8f6f4 v[122:125], v[26:33], v[50:57], v[122:125]
	v_mfma_f32_16x16x128_f8f6f4 v[110:113], v[18:25], v[58:65], v[110:113]
	v_mfma_f32_16x16x128_f8f6f4 v[106:109], v[26:33], v[58:65], v[106:109]
	s_setprio 0
	s_barrier
	ds_read_b128 v[42:45], v169 offset:49152
	ds_read_b128 v[46:49], v169 offset:50176
	ds_read_b128 v[58:61], v169 offset:51200
	ds_read_b128 v[62:65], v169 offset:52224
	ds_read_b128 v[170:173], v169 offset:53248
	ds_read_b128 v[174:177], v169 offset:54272
	ds_read_b128 v[178:181], v169 offset:55296
	ds_read_b128 v[182:185], v169 offset:56320
	s_add_i32 s38, s74, 0x18000
	s_mov_b32 m0, s38
	s_nop 0
	global_load_lds_dwordx4 v166, s[36:37]
	s_add_i32 s38, s74, 0x1a000
	s_mov_b32 m0, s38
	s_nop 0
	global_load_lds_dwordx4 v167, s[36:37]
	s_add_u32 s34, s34, 0x2080
	s_addc_u32 s35, s35, 0
	s_add_i32 s36, s74, 0x1c000
	s_mov_b32 m0, s36
	s_nop 0
	global_load_lds_dwordx4 v166, s[34:35]
	s_add_i32 s36, s74, 0x1e000
	s_mov_b32 m0, s36
	s_nop 0
	global_load_lds_dwordx4 v167, s[34:35]
	s_and_b64 vcc, exec, s[18:19]
	s_cbranch_vccnz .Lmy_w9a1
	s_waitcnt vmcnt(6)
.Lmy_w9a1:
	s_waitcnt lgkmcnt(0)
	s_barrier
	s_setprio 1
	s_waitcnt lgkmcnt(6)
	v_mfma_f32_16x16x128_f8f6f4 v[86:89], v[2:9], v[42:49], v[86:89]
	v_mfma_f32_16x16x128_f8f6f4 v[82:85], v[10:17], v[42:49], v[82:85]
	s_waitcnt lgkmcnt(4)
	v_mfma_f32_16x16x128_f8f6f4 v[70:73], v[2:9], v[58:65], v[70:73]
	v_mfma_f32_16x16x128_f8f6f4 v[66:69], v[10:17], v[58:65], v[66:69]
	s_waitcnt lgkmcnt(2)
	v_mfma_f32_16x16x128_f8f6f4 v[54:57], v[2:9], v[170:177], v[202:205]
	v_mfma_f32_16x16x128_f8f6f4 v[50:53], v[10:17], v[170:177], v[206:209]
	s_waitcnt lgkmcnt(0)
	v_mfma_f32_16x16x128_f8f6f4 v[38:41], v[2:9], v[178:185], v[210:213]
	v_mfma_f32_16x16x128_f8f6f4 v[34:37], v[10:17], v[178:185], v[214:217]
	v_mfma_f32_16x16x128_f8f6f4 v[94:97], v[18:25], v[42:49], v[94:97]
	v_mfma_f32_16x16x128_f8f6f4 v[90:93], v[26:33], v[42:49], v[90:93]
	v_mfma_f32_16x16x128_f8f6f4 v[78:81], v[18:25], v[58:65], v[78:81]
	v_mfma_f32_16x16x128_f8f6f4 v[74:77], v[26:33], v[58:65], v[74:77]
	v_mfma_f32_16x16x128_f8f6f4 v[62:65], v[18:25], v[170:177], v[218:221]
	v_mfma_f32_16x16x128_f8f6f4 v[58:61], v[26:33], v[170:177], v[186:189]
	v_mfma_f32_16x16x128_f8f6f4 v[46:49], v[18:25], v[178:185], v[190:193]
	v_mfma_f32_16x16x128_f8f6f4 v[42:45], v[26:33], v[178:185], v[194:197]
	s_setprio 0
	s_and_b64 vcc, exec, s[18:19]
	s_cbranch_vccz .Lmy_w9b1
	s_waitcnt vmcnt(6)
.Lmy_w9b1:
	s_barrier
	s_add_i32 s73, s73, 2
	s_add_u32 s25, s25, 0x100
	s_addc_u32 s71, s71, 0
	s_add_u32 s26, s26, 0x100
	s_addc_u32 s27, s27, 0
	s_cmp_gt_u32 s73, 5
	s_cbranch_scc1 .LBB0_1065

; #define PG8_STAGE(bufoff, gbase, voff) do { PG8_GLDS((const char*)(gbase), (voff)[0], ldsb + (bufoff)); PG8_GLDS((const char*)(gbase), (voff)[1], ldsb + (bufoff) + 8192u); } while (0)
; #define PG8_STAGEA(bufoff, gbase, o0, o1) do { PG8_GLDS((const char*)(gbase), (o0), ldsb + (bufoff)); PG8_GLDS((const char*)(gbase), (o1), ldsb + (bufoff) + 8192u); } while (0)
; #define PG8_LDA(dst, b, h) do { if constexpr (F8) { _Pragma("unroll") for (int m = 0; m < 4; ++m) dst##8[m] = PG8_LD32(lds + PG8_SA(b, h) + aoff + m * 2048); } else { \
;         _Pragma("unroll") for (int m = 0; m < 4; ++m) _Pragma("unroll") for (int k = 0; k < 2; ++k) dst[m][k] = *(const LAS bf16x8*)(lds + PG8_SA(b, h) + aoff + m * 2048 + k * 1024); } } while (0)
; #define PG8_WAIT_VX() do { if (relax) asm volatile("s_waitcnt vmcnt(%0)" :: "n"(8 + Epi::RELAX) : "memory"); else PG8_WAIT_V(8); } while (0)
; #define PG8_WAIT_L(n) asm volatile("s_waitcnt lgkmcnt(" #n ")" ::: "memory")
; #define PG8_BAR __builtin_amdgcn_s_barrier()
; #define PG8_SCHED __builtin_amdgcn_sched_barrier(0)
; template <class Epi, class Sched, bool F8 = false, bool PF = false, bool I8 = false, int PID = -1>
; __device__ __forceinline__ void gemm_phase(LAS unsigned char* lds, LAS unsigned char* xlds, const int RP, const int RPB, const int nt, const Sched& S, const Epi& E, const int stagger_ticks) {
;     ...
;             PG8_WAIT_VX(); PG8_WAIT_L(0); PG8_BAR; PG8_MMA(0, 0, At, B0); PG8_MMA(0, 1, At, B1); PG8_BAR; PG8_SCHED;
;             if constexpr (Epi::BIAS_DMA) { if (t == 0 && has_next) E.bias_dma(nxt, xlds + 8192 + ((ui + 1) & 1) * Epi::BIAS_STRIDE, wid, lane); }
;             PG8_LDA(At, 0, 1); PG8_STAGE(PG8_SB(0, 0), b2, voffB); PG8_STAGE(PG8_SB(0, 1), b2 + hstepB, voffB); PG8_STAGEA(PG8_SA(0, 0), a2, vA0, vA1);
;             PG8_WAIT_VX(); PG8_WAIT_L(0); PG8_BAR; PG8_MMA(1, 0, At, B0); PG8_MMA(1, 1, At, B1); PG8_BAR; PG8_SCHED;
.Lmy_w9a2:
	s_waitcnt lgkmcnt(0)
	s_barrier
	s_setprio 1
	s_waitcnt lgkmcnt(6)
	v_mfma_f32_16x16x128_f8f6f4 v[86:89], v[2:9], v[170:177], 0
	v_mfma_f32_16x16x128_f8f6f4 v[82:85], v[10:17], v[170:177], 0
	s_waitcnt lgkmcnt(4)
	v_mfma_f32_16x16x128_f8f6f4 v[70:73], v[2:9], v[178:185], 0
	v_mfma_f32_16x16x128_f8f6f4 v[66:69], v[10:17], v[178:185], 0
	s_waitcnt lgkmcnt(2)
	v_mfma_f32_16x16x128_f8f6f4 v[202:205], v[2:9], v[186:193], 0
	v_mfma_f32_16x16x128_f8f6f4 v[206:209], v[10:17], v[186:193], 0
	s_waitcnt lgkmcnt(0)
	v_mfma_f32_16x16x128_f8f6f4 v[210:213], v[2:9], v[194:201], 0
	v_mfma_f32_16x16x128_f8f6f4 v[214:217], v[10:17], v[194:201], 0
	v_mfma_f32_16x16x128_f8f6f4 v[94:97], v[18:25], v[170:177], 0
	v_mfma_f32_16x16x128_f8f6f4 v[90:93], v[26:33], v[170:177], 0
	v_mfma_f32_16x16x128_f8f6f4 v[78:81], v[18:25], v[178:185], 0
	v_mfma_f32_16x16x128_f8f6f4 v[74:77], v[26:33], v[178:185], 0
	v_mfma_f32_16x16x128_f8f6f4 v[218:221], v[18:25], v[186:193], 0
	v_mfma_f32_16x16x128_f8f6f4 v[186:189], v[26:33], v[186:193], 0
	v_mfma_f32_16x16x128_f8f6f4 v[190:193], v[18:25], v[194:201], 0
	v_mfma_f32_16x16x128_f8f6f4 v[194:197], v[26:33], v[194:201], 0
	s_setprio 0
	s_and_b64 vcc, exec, s[18:19]
	s_cbranch_vccz .Lmy_w9b2
	s_waitcnt vmcnt(6)

; #define PG8_STAGE(bufoff, gbase, voff) do { PG8_GLDS((const char*)(gbase), (voff)[0], ldsb + (bufoff)); PG8_GLDS((const char*)(gbase), (voff)[1], ldsb + (bufoff) + 8192u); } while (0)
; #define PG8_STAGEA(bufoff, gbase, o0, o1) do { PG8_GLDS((const char*)(gbase), (o0), ldsb + (bufoff)); PG8_GLDS((const char*)(gbase), (o1), ldsb + (bufoff) + 8192u); } while (0)
; #define PG8_STAGEA1(bufoff, gbase) do { if constexpr (Sched::GATHER) { PG8_STAGEA(bufoff, gbase, vA2, vA3); } else { PG8_STAGEA(bufoff, (gbase) + hstep, vA0, vA1); } } while (0)
; #define PG8_LDA(dst, b, h) do { if constexpr (F8) { _Pragma("unroll") for (int m = 0; m < 4; ++m) dst##8[m] = PG8_LD32(lds + PG8_SA(b, h) + aoff + m * 2048); } else { \
;         _Pragma("unroll") for (int m = 0; m < 4; ++m) _Pragma("unroll") for (int k = 0; k < 2; ++k) dst[m][k] = *(const LAS bf16x8*)(lds + PG8_SA(b, h) + aoff + m * 2048 + k * 1024); } } while (0)
; #define PG8_LDB(dst, b, h) do { if constexpr (F8) { _Pragma("unroll") for (int n = 0; n < 2; ++n) dst##8[n] = PG8_LD32(lds + PG8_SB(b, h) + boff + n * 2048); } else { \
;         _Pragma("unroll") for (int n = 0; n < 2; ++n) _Pragma("unroll") for (int k = 0; k < 2; ++k) dst[n][k] = *(const LAS bf16x8*)(lds + PG8_SB(b, h) + boff + n * 2048 + k * 1024); } } while (0)
; #define PG8_WAIT_VR() PG8_WAIT_V(8)
; #define PG8_WAIT_VX() do { if (relax) asm volatile("s_waitcnt vmcnt(%0)" :: "n"(8 + Epi::RELAX) : "memory"); else PG8_WAIT_V(8); } while (0)
; template <class Epi, class Sched, bool F8 = false, bool PF = false, bool I8 = false, int PID = -1>
; __device__ __forceinline__ void gemm_phase(LAS unsigned char* lds, LAS unsigned char* xlds, const int RP, const int RPB, const int nt, const Sched& S, const Epi& E, const int stagger_ticks) {
;     ...
;             PG8_WAIT_VX(); PG8_WAIT_L(0); PG8_BAR; PG8_MMA(1, 0, At, B0); PG8_MMA(1, 1, At, B1); PG8_BAR; PG8_SCHED;
;             PG8_LDB(B0, 1, 0); PG8_LDB(B1, 1, 1); PG8_SCHED; PG8_LDA(At, 1, 0); PG8_STAGEA1(PG8_SA(0, 1), a2);
;             PG8_WAIT_VR(); PG8_WAIT_L(0); PG8_BAR; PG8_MMA(0, 0, At, B0); PG8_MMA(0, 1, At, B1); PG8_BAR; PG8_SCHED;
;             PG8_LDA(At, 1, 1); PG8_STAGE(PG8_SB(1, 0), b3, voffB); PG8_STAGE(PG8_SB(1, 1), b3 + hstepB, voffB); PG8_STAGEA(PG8_SA(1, 0), a3, vA0, vA1);
;             PG8_WAIT_VR(); PG8_WAIT_L(0); PG8_BAR; PG8_MMA(1, 0, At, B0); PG8_MMA(1, 1, At, B1); PG8_BAR; PG8_SCHED;
;         }
.Lmy_w9b3:
	s_barrier
	s_add_i32 s73, s73, 2
	s_add_u32 s25, s25, 0x100
	s_addc_u32 s71, s71, 0
	s_add_u32 s26, s26, 0x100
	s_addc_u32 s27, s27, 0
	s_cmp_gt_u32 s73, 5
	s_branch .LBB0_1063
